# GLA pre-pass: log-sigmoid tail fused to one fma per site, dead zero-subtract removed, redundant nops dropped (on top of v54)
# speedup vs baseline: 1.0169x; 1.0028x over previous
.LBB0_411:
	s_waitcnt vmcnt(14)
	v_readlane_b32 s40, v70, 0
	v_readlane_b32 s41, v71, 0
	s_lshl_b32 s2, s40, 16
	s_and_b32 s40, s40, 0xffff0000
	v_pk_mul_f32 v[74:75], v[4:5], s[40:41] op_sel_hi:[1,0]
	v_pk_mul_f32 v[76:77], v[2:3], s[40:41] op_sel_hi:[1,0]
	s_and_b32 s40, s41, 0xffff0000
	v_readlane_b32 s58, v72, 0
	v_pk_fma_f32 v[74:75], v[28:29], s[2:3], v[74:75] op_sel_hi:[1,0,1]
	v_pk_fma_f32 v[76:77], v[26:27], s[2:3], v[76:77] op_sel_hi:[1,0,1]
	s_lshl_b32 s2, s41, 16
	v_pk_mul_f32 v[80:81], v[10:11], s[40:41] op_sel_hi:[1,0]
	v_pk_add_f32 v[76:77], v[66:67], v[76:77]
	v_pk_mul_f32 v[78:79], v[12:13], s[40:41] op_sel_hi:[1,0]
	v_pk_fma_f32 v[80:81], v[6:7], s[2:3], v[80:81] op_sel_hi:[1,0,1]
	s_and_b32 s40, s58, 0xffff0000
	v_readlane_b32 s66, v73, 0
	v_pk_add_f32 v[74:75], v[68:69], v[74:75]
	v_pk_fma_f32 v[78:79], v[8:9], s[2:3], v[78:79] op_sel_hi:[1,0,1]
	v_pk_add_f32 v[76:77], v[76:77], v[80:81]
	s_lshl_b32 s2, s58, 16
	v_pk_mul_f32 v[80:81], v[18:19], s[40:41] op_sel_hi:[1,0]
	v_pk_add_f32 v[74:75], v[74:75], v[78:79]
	v_pk_mul_f32 v[78:79], v[20:21], s[40:41] op_sel_hi:[1,0]
	v_pk_fma_f32 v[80:81], v[14:15], s[2:3], v[80:81] op_sel_hi:[1,0,1]
	s_and_b32 s40, s66, 0xffff0000
	v_readlane_b32 s67, v70, 1
	v_pk_fma_f32 v[78:79], v[16:17], s[2:3], v[78:79] op_sel_hi:[1,0,1]
	v_pk_add_f32 v[76:77], v[76:77], v[80:81]
	s_lshl_b32 s2, s66, 16
	v_pk_mul_f32 v[80:81], v[30:31], s[40:41] op_sel_hi:[1,0]
	v_pk_add_f32 v[74:75], v[74:75], v[78:79]
	v_pk_mul_f32 v[78:79], v[32:33], s[40:41] op_sel_hi:[1,0]
	v_pk_fma_f32 v[80:81], v[22:23], s[2:3], v[80:81] op_sel_hi:[1,0,1]
	s_and_b32 s40, s67, 0xffff0000
	v_readlane_b32 s73, v71, 1
	v_pk_fma_f32 v[78:79], v[24:25], s[2:3], v[78:79] op_sel_hi:[1,0,1]
	v_pk_add_f32 v[76:77], v[76:77], v[80:81]
	s_lshl_b32 s2, s67, 16
	v_pk_mul_f32 v[80:81], v[38:39], s[40:41] op_sel_hi:[1,0]
	v_pk_add_f32 v[74:75], v[74:75], v[78:79]
	v_pk_mul_f32 v[78:79], v[40:41], s[40:41] op_sel_hi:[1,0]
	v_pk_fma_f32 v[80:81], v[34:35], s[2:3], v[80:81] op_sel_hi:[1,0,1]
	s_and_b32 s40, s73, 0xffff0000
	v_readlane_b32 s74, v72, 1
	v_pk_fma_f32 v[78:79], v[36:37], s[2:3], v[78:79] op_sel_hi:[1,0,1]
	v_pk_add_f32 v[76:77], v[76:77], v[80:81]
	s_lshl_b32 s2, s73, 16
	v_pk_mul_f32 v[80:81], v[46:47], s[40:41] op_sel_hi:[1,0]
	v_pk_add_f32 v[74:75], v[74:75], v[78:79]
	v_pk_mul_f32 v[78:79], v[48:49], s[40:41] op_sel_hi:[1,0]
	v_pk_fma_f32 v[80:81], v[42:43], s[2:3], v[80:81] op_sel_hi:[1,0,1]
	s_and_b32 s40, s74, 0xffff0000
	v_readlane_b32 s75, v73, 1
	v_pk_fma_f32 v[78:79], v[44:45], s[2:3], v[78:79] op_sel_hi:[1,0,1]
	v_pk_add_f32 v[76:77], v[76:77], v[80:81]
	s_lshl_b32 s2, s74, 16
	v_pk_mul_f32 v[80:81], v[54:55], s[40:41] op_sel_hi:[1,0]
	s_and_b32 s58, s75, 0xffff0000
	v_pk_fma_f32 v[80:81], v[50:51], s[2:3], v[80:81] op_sel_hi:[1,0,1]
	v_pk_add_f32 v[74:75], v[74:75], v[78:79]
	v_pk_mul_f32 v[78:79], v[56:57], s[40:41] op_sel_hi:[1,0]
	v_pk_add_f32 v[76:77], v[76:77], v[80:81]
	s_lshl_b32 s40, s75, 16
	v_pk_mul_f32 v[80:81], v[62:63], s[58:59] op_sel_hi:[1,0]
	v_pk_fma_f32 v[78:79], v[52:53], s[2:3], v[78:79] op_sel_hi:[1,0,1]
	v_pk_fma_f32 v[80:81], v[58:59], s[40:41], v[80:81] op_sel_hi:[1,0,1]
	v_pk_add_f32 v[74:75], v[74:75], v[78:79]
	v_pk_add_f32 v[76:77], v[76:77], v[80:81]
	v_pk_mul_f32 v[78:79], v[64:65], s[58:59] op_sel_hi:[1,0]
	v_mul_f32_e64 v80, |v76|, s53
	v_exp_f32_e32 v80, v80
	v_pk_fma_f32 v[78:79], v[60:61], s[40:41], v[78:79] op_sel_hi:[1,0,1]
	v_readlane_b32 s58, v72, 2
	v_pk_add_f32 v[78:79], v[74:75], v[78:79]
	v_add_f32_e32 v80, 1.0, v80
	v_min_f32_e32 v74, 0, v76
	v_mul_f32_e64 v76, |v77|, s53
	v_log_f32_e32 v80, v80
	v_exp_f32_e32 v76, v76
	v_readlane_b32 s66, v73, 2
	v_readlane_b32 s67, v70, 3
	v_readlane_b32 s73, v71, 3
	v_readlane_b32 s74, v72, 3
	v_fma_f32 v74, -v80, s69, v74
	v_add_f32_e32 v75, 1.0, v76
	v_readlane_b32 s75, v73, 3
	v_mul_f32_e32 v74, 0x3d800000, v74
	v_log_f32_e32 v75, v75
	v_min_f32_e32 v76, 0, v77
	v_max_f32_e32 v74, -1.0, v74
	v_and_b32_e32 v196, 0xffff0000, v105
	v_mul_f32_e64 v77, |v78|, s53
	v_exp_f32_e32 v77, v77
	v_fma_f32 v75, -v75, s69, v76
	v_mul_f32_e32 v75, 0x3d800000, v75
	v_add_f32_e32 v76, 1.0, v77
	v_max_f32_e32 v75, -1.0, v75
	v_log_f32_e32 v76, v76
	v_min_f32_e32 v77, 0, v78
	v_mul_f32_e64 v78, |v79|, s53
	v_exp_f32_e32 v78, v78
	v_fma_f32 v76, -v76, s69, v77
	v_mul_f32_e32 v76, 0x3d800000, v76
	v_add_f32_e32 v77, 1.0, v78
	v_max_f32_e32 v76, -1.0, v76
	v_log_f32_e32 v77, v77
	v_min_f32_e32 v78, 0, v79
	v_readlane_b32 s40, v70, 2
	v_readlane_b32 s41, v71, 2
	s_lshl_b32 s2, s40, 16
	s_and_b32 s40, s40, 0xffff0000
	v_fma_f32 v77, -v77, s69, v78
	v_pk_mul_f32 v[78:79], v[4:5], s[40:41] op_sel_hi:[1,0]
	v_pk_mul_f32 v[80:81], v[2:3], s[40:41] op_sel_hi:[1,0]
	s_and_b32 s40, s41, 0xffff0000
	v_pk_fma_f32 v[78:79], v[28:29], s[2:3], v[78:79] op_sel_hi:[1,0,1]
	v_pk_fma_f32 v[80:81], v[26:27], s[2:3], v[80:81] op_sel_hi:[1,0,1]
	s_lshl_b32 s2, s41, 16
	v_pk_mul_f32 v[152:153], v[10:11], s[40:41] op_sel_hi:[1,0]
	v_pk_add_f32 v[80:81], v[66:67], v[80:81]
	v_pk_mul_f32 v[150:151], v[12:13], s[40:41] op_sel_hi:[1,0]
	v_pk_fma_f32 v[152:153], v[6:7], s[2:3], v[152:153] op_sel_hi:[1,0,1]
	s_and_b32 s40, s58, 0xffff0000
	v_pk_add_f32 v[78:79], v[68:69], v[78:79]
	v_pk_fma_f32 v[150:151], v[8:9], s[2:3], v[150:151] op_sel_hi:[1,0,1]
	v_pk_add_f32 v[80:81], v[80:81], v[152:153]
	s_lshl_b32 s2, s58, 16
	v_pk_mul_f32 v[152:153], v[18:19], s[40:41] op_sel_hi:[1,0]
	v_pk_add_f32 v[78:79], v[78:79], v[150:151]
	v_pk_mul_f32 v[150:151], v[20:21], s[40:41] op_sel_hi:[1,0]
	v_pk_fma_f32 v[152:153], v[14:15], s[2:3], v[152:153] op_sel_hi:[1,0,1]
	s_and_b32 s40, s66, 0xffff0000
	v_pk_fma_f32 v[150:151], v[16:17], s[2:3], v[150:151] op_sel_hi:[1,0,1]
	v_pk_add_f32 v[80:81], v[80:81], v[152:153]
	s_lshl_b32 s2, s66, 16
	v_pk_mul_f32 v[152:153], v[30:31], s[40:41] op_sel_hi:[1,0]
	v_pk_add_f32 v[78:79], v[78:79], v[150:151]
	v_pk_mul_f32 v[150:151], v[32:33], s[40:41] op_sel_hi:[1,0]
	v_pk_fma_f32 v[152:153], v[22:23], s[2:3], v[152:153] op_sel_hi:[1,0,1]
	s_and_b32 s40, s67, 0xffff0000
	v_pk_fma_f32 v[150:151], v[24:25], s[2:3], v[150:151] op_sel_hi:[1,0,1]
	v_pk_add_f32 v[80:81], v[80:81], v[152:153]
	s_lshl_b32 s2, s67, 16
	v_pk_mul_f32 v[152:153], v[38:39], s[40:41] op_sel_hi:[1,0]
	v_pk_add_f32 v[78:79], v[78:79], v[150:151]
	v_pk_mul_f32 v[150:151], v[40:41], s[40:41] op_sel_hi:[1,0]
	v_pk_fma_f32 v[152:153], v[34:35], s[2:3], v[152:153] op_sel_hi:[1,0,1]
	s_and_b32 s40, s73, 0xffff0000
	v_pk_fma_f32 v[150:151], v[36:37], s[2:3], v[150:151] op_sel_hi:[1,0,1]
	v_pk_add_f32 v[80:81], v[80:81], v[152:153]
	s_lshl_b32 s2, s73, 16
	v_pk_mul_f32 v[152:153], v[46:47], s[40:41] op_sel_hi:[1,0]
	v_pk_add_f32 v[78:79], v[78:79], v[150:151]
	v_pk_mul_f32 v[150:151], v[48:49], s[40:41] op_sel_hi:[1,0]
	v_pk_fma_f32 v[152:153], v[42:43], s[2:3], v[152:153] op_sel_hi:[1,0,1]
	s_and_b32 s40, s74, 0xffff0000
	v_pk_fma_f32 v[150:151], v[44:45], s[2:3], v[150:151] op_sel_hi:[1,0,1]
	v_pk_add_f32 v[80:81], v[80:81], v[152:153]
	s_lshl_b32 s2, s74, 16
	v_pk_mul_f32 v[152:153], v[54:55], s[40:41] op_sel_hi:[1,0]
	s_and_b32 s58, s75, 0xffff0000
	v_pk_fma_f32 v[152:153], v[50:51], s[2:3], v[152:153] op_sel_hi:[1,0,1]
	v_pk_add_f32 v[78:79], v[78:79], v[150:151]
	v_pk_mul_f32 v[150:151], v[56:57], s[40:41] op_sel_hi:[1,0]
	v_pk_add_f32 v[80:81], v[80:81], v[152:153]
	s_lshl_b32 s40, s75, 16
	v_pk_mul_f32 v[152:153], v[62:63], s[58:59] op_sel_hi:[1,0]
	v_pk_fma_f32 v[150:151], v[52:53], s[2:3], v[150:151] op_sel_hi:[1,0,1]
	v_pk_fma_f32 v[152:153], v[58:59], s[40:41], v[152:153] op_sel_hi:[1,0,1]
	v_pk_add_f32 v[78:79], v[78:79], v[150:151]
	v_pk_add_f32 v[80:81], v[80:81], v[152:153]
	v_pk_mul_f32 v[150:151], v[64:65], s[58:59] op_sel_hi:[1,0]
	v_mul_f32_e64 v152, |v80|, s53
	v_exp_f32_e32 v152, v152
	v_pk_fma_f32 v[150:151], v[60:61], s[40:41], v[150:151] op_sel_hi:[1,0,1]
	v_min_f32_e32 v80, 0, v80
	v_pk_add_f32 v[78:79], v[78:79], v[150:151]
	v_add_f32_e32 v152, 1.0, v152
	v_mul_f32_e64 v151, |v81|, s53
	v_exp_f32_e32 v151, v151
	v_log_f32_e32 v152, v152
	v_min_f32_e32 v81, 0, v81
	v_readlane_b32 s58, v72, 4
	v_readlane_b32 s66, v73, 4
	v_readlane_b32 s67, v70, 5
	v_readlane_b32 s73, v71, 5
	v_fma_f32 v80, -v152, s69, v80
	v_add_f32_e32 v150, 1.0, v151
	v_readlane_b32 s74, v72, 5
	v_readlane_b32 s75, v73, 5
	v_log_f32_e32 v150, v150
	v_mul_f32_e32 v80, 0x3d800000, v80
	v_max_f32_e32 v80, -1.0, v80
	v_mul_f32_e32 v77, 0x3d800000, v77
	v_max_f32_e32 v77, -1.0, v77
	v_mul_f32_e64 v151, |v78|, s53
	v_exp_f32_e32 v151, v151
	v_fma_f32 v81, -v150, s69, v81
	v_min_f32_e32 v78, 0, v78
	v_add_f32_e32 v150, 1.0, v151
	v_mul_f32_e32 v81, 0x3d800000, v81
	v_max_f32_e32 v81, -1.0, v81
	v_log_f32_e32 v150, v150
	v_pk_add_f32 v[190:191], v[76:77], 0 op_sel_hi:[1,0]
	v_mul_f32_e64 v151, |v79|, s53
	v_exp_f32_e32 v151, v151
	v_fma_f32 v78, -v150, s69, v78
	v_min_f32_e32 v79, 0, v79
	v_add_f32_e32 v150, 1.0, v151
	v_mul_f32_e32 v78, 0x3d800000, v78
	v_max_f32_e32 v78, -1.0, v78
	v_log_f32_e32 v150, v150
	v_readlane_b32 s40, v70, 4
	v_readlane_b32 s41, v71, 4
	s_lshl_b32 s2, s40, 16
	s_and_b32 s40, s40, 0xffff0000
	v_fma_f32 v79, -v150, s69, v79
	v_pk_mul_f32 v[150:151], v[4:5], s[40:41] op_sel_hi:[1,0]
	v_pk_mul_f32 v[152:153], v[2:3], s[40:41] op_sel_hi:[1,0]
	s_and_b32 s40, s41, 0xffff0000
	v_pk_fma_f32 v[150:151], v[28:29], s[2:3], v[150:151] op_sel_hi:[1,0,1]
	v_pk_fma_f32 v[152:153], v[26:27], s[2:3], v[152:153] op_sel_hi:[1,0,1]
	s_lshl_b32 s2, s41, 16
	v_pk_mul_f32 v[156:157], v[10:11], s[40:41] op_sel_hi:[1,0]
	v_pk_add_f32 v[152:153], v[66:67], v[152:153]
	v_pk_mul_f32 v[154:155], v[12:13], s[40:41] op_sel_hi:[1,0]
	v_pk_fma_f32 v[156:157], v[6:7], s[2:3], v[156:157] op_sel_hi:[1,0,1]
	s_and_b32 s40, s58, 0xffff0000
	v_pk_add_f32 v[150:151], v[68:69], v[150:151]
	v_pk_fma_f32 v[154:155], v[8:9], s[2:3], v[154:155] op_sel_hi:[1,0,1]
	v_pk_add_f32 v[152:153], v[152:153], v[156:157]
	s_lshl_b32 s2, s58, 16
	v_pk_mul_f32 v[156:157], v[18:19], s[40:41] op_sel_hi:[1,0]
	v_pk_add_f32 v[150:151], v[150:151], v[154:155]
	v_pk_mul_f32 v[154:155], v[20:21], s[40:41] op_sel_hi:[1,0]
	v_pk_fma_f32 v[156:157], v[14:15], s[2:3], v[156:157] op_sel_hi:[1,0,1]
	s_and_b32 s40, s66, 0xffff0000
	v_pk_fma_f32 v[154:155], v[16:17], s[2:3], v[154:155] op_sel_hi:[1,0,1]
	v_pk_add_f32 v[152:153], v[152:153], v[156:157]
	s_lshl_b32 s2, s66, 16
	v_pk_mul_f32 v[156:157], v[30:31], s[40:41] op_sel_hi:[1,0]
	v_pk_add_f32 v[150:151], v[150:151], v[154:155]
	v_pk_mul_f32 v[154:155], v[32:33], s[40:41] op_sel_hi:[1,0]
	v_pk_fma_f32 v[156:157], v[22:23], s[2:3], v[156:157] op_sel_hi:[1,0,1]
	s_and_b32 s40, s67, 0xffff0000
	v_pk_fma_f32 v[154:155], v[24:25], s[2:3], v[154:155] op_sel_hi:[1,0,1]
	v_pk_add_f32 v[152:153], v[152:153], v[156:157]
	s_lshl_b32 s2, s67, 16
	v_pk_mul_f32 v[156:157], v[38:39], s[40:41] op_sel_hi:[1,0]
	v_pk_add_f32 v[150:151], v[150:151], v[154:155]
	v_pk_mul_f32 v[154:155], v[40:41], s[40:41] op_sel_hi:[1,0]
	v_pk_fma_f32 v[156:157], v[34:35], s[2:3], v[156:157] op_sel_hi:[1,0,1]
	s_and_b32 s40, s73, 0xffff0000
	v_pk_fma_f32 v[154:155], v[36:37], s[2:3], v[154:155] op_sel_hi:[1,0,1]
	v_pk_add_f32 v[152:153], v[152:153], v[156:157]
	s_lshl_b32 s2, s73, 16
	v_pk_mul_f32 v[156:157], v[46:47], s[40:41] op_sel_hi:[1,0]
	v_pk_add_f32 v[150:151], v[150:151], v[154:155]
	v_pk_mul_f32 v[154:155], v[48:49], s[40:41] op_sel_hi:[1,0]
	v_pk_fma_f32 v[156:157], v[42:43], s[2:3], v[156:157] op_sel_hi:[1,0,1]
	s_and_b32 s40, s74, 0xffff0000
	v_pk_fma_f32 v[154:155], v[44:45], s[2:3], v[154:155] op_sel_hi:[1,0,1]
	v_pk_add_f32 v[152:153], v[152:153], v[156:157]
	s_lshl_b32 s2, s74, 16
	v_pk_mul_f32 v[156:157], v[54:55], s[40:41] op_sel_hi:[1,0]
	s_and_b32 s58, s75, 0xffff0000
	v_pk_fma_f32 v[156:157], v[50:51], s[2:3], v[156:157] op_sel_hi:[1,0,1]
	v_pk_add_f32 v[150:151], v[150:151], v[154:155]
	v_pk_mul_f32 v[154:155], v[56:57], s[40:41] op_sel_hi:[1,0]
	v_pk_add_f32 v[152:153], v[152:153], v[156:157]
	s_lshl_b32 s40, s75, 16
	v_pk_mul_f32 v[156:157], v[62:63], s[58:59] op_sel_hi:[1,0]
	v_pk_fma_f32 v[154:155], v[52:53], s[2:3], v[154:155] op_sel_hi:[1,0,1]
	v_pk_fma_f32 v[156:157], v[58:59], s[40:41], v[156:157] op_sel_hi:[1,0,1]
	v_pk_add_f32 v[150:151], v[150:151], v[154:155]
	v_pk_add_f32 v[152:153], v[152:153], v[156:157]
	v_pk_mul_f32 v[154:155], v[64:65], s[58:59] op_sel_hi:[1,0]
	v_mul_f32_e64 v156, |v152|, s53
	v_exp_f32_e32 v156, v156
	v_pk_fma_f32 v[154:155], v[60:61], s[40:41], v[154:155] op_sel_hi:[1,0,1]
	v_min_f32_e32 v152, 0, v152
	v_pk_add_f32 v[150:151], v[150:151], v[154:155]
	v_add_f32_e32 v156, 1.0, v156
	v_mul_f32_e64 v155, |v153|, s53
	v_exp_f32_e32 v155, v155
	v_log_f32_e32 v156, v156
	v_min_f32_e32 v153, 0, v153
	v_readlane_b32 s58, v72, 6
	v_readlane_b32 s66, v73, 6
	v_readlane_b32 s67, v70, 7
	v_readlane_b32 s73, v71, 7
	v_fma_f32 v152, -v156, s69, v152
	v_add_f32_e32 v154, 1.0, v155
	v_readlane_b32 s74, v72, 7
	v_readlane_b32 s75, v73, 7
	v_log_f32_e32 v154, v154
	v_mul_f32_e32 v152, 0x3d800000, v152
	v_max_f32_e32 v152, -1.0, v152
	v_mul_f32_e32 v79, 0x3d800000, v79
	v_max_f32_e32 v79, -1.0, v79
	v_mul_f32_e64 v155, |v150|, s53
	v_exp_f32_e32 v155, v155
	v_fma_f32 v153, -v154, s69, v153
	v_min_f32_e32 v150, 0, v150
	v_add_f32_e32 v154, 1.0, v155
	v_mul_f32_e32 v153, 0x3d800000, v153
	v_max_f32_e32 v153, -1.0, v153
	v_log_f32_e32 v154, v154
	v_mul_f32_e64 v155, |v151|, s53
	v_exp_f32_e32 v155, v155
	v_fma_f32 v150, -v154, s69, v150
	v_min_f32_e32 v151, 0, v151
	v_add_f32_e32 v154, 1.0, v155
	v_mul_f32_e32 v150, 0x3d800000, v150
	v_max_f32_e32 v150, -1.0, v150
	v_log_f32_e32 v154, v154
	v_readlane_b32 s40, v70, 6
	v_readlane_b32 s41, v71, 6
	s_lshl_b32 s2, s40, 16
	s_and_b32 s40, s40, 0xffff0000
	v_fma_f32 v151, -v154, s69, v151
	v_pk_mul_f32 v[154:155], v[4:5], s[40:41] op_sel_hi:[1,0]
	v_pk_mul_f32 v[156:157], v[2:3], s[40:41] op_sel_hi:[1,0]
	s_and_b32 s40, s41, 0xffff0000
	v_pk_fma_f32 v[154:155], v[28:29], s[2:3], v[154:155] op_sel_hi:[1,0,1]
	v_pk_fma_f32 v[156:157], v[26:27], s[2:3], v[156:157] op_sel_hi:[1,0,1]
	s_lshl_b32 s2, s41, 16
	v_pk_mul_f32 v[160:161], v[10:11], s[40:41] op_sel_hi:[1,0]
	v_pk_add_f32 v[156:157], v[66:67], v[156:157]
	v_pk_mul_f32 v[158:159], v[12:13], s[40:41] op_sel_hi:[1,0]
	v_pk_fma_f32 v[160:161], v[6:7], s[2:3], v[160:161] op_sel_hi:[1,0,1]
	s_and_b32 s40, s58, 0xffff0000
	v_pk_add_f32 v[154:155], v[68:69], v[154:155]
	v_pk_fma_f32 v[158:159], v[8:9], s[2:3], v[158:159] op_sel_hi:[1,0,1]
	v_pk_add_f32 v[156:157], v[156:157], v[160:161]
	s_lshl_b32 s2, s58, 16
	v_pk_mul_f32 v[160:161], v[18:19], s[40:41] op_sel_hi:[1,0]
	v_pk_add_f32 v[154:155], v[154:155], v[158:159]
	v_pk_mul_f32 v[158:159], v[20:21], s[40:41] op_sel_hi:[1,0]
	v_pk_fma_f32 v[160:161], v[14:15], s[2:3], v[160:161] op_sel_hi:[1,0,1]
	s_and_b32 s40, s66, 0xffff0000
	v_pk_fma_f32 v[158:159], v[16:17], s[2:3], v[158:159] op_sel_hi:[1,0,1]
	v_pk_add_f32 v[156:157], v[156:157], v[160:161]
	s_lshl_b32 s2, s66, 16
	v_pk_mul_f32 v[160:161], v[30:31], s[40:41] op_sel_hi:[1,0]
	v_pk_add_f32 v[154:155], v[154:155], v[158:159]
	v_pk_mul_f32 v[158:159], v[32:33], s[40:41] op_sel_hi:[1,0]
	v_pk_fma_f32 v[160:161], v[22:23], s[2:3], v[160:161] op_sel_hi:[1,0,1]
	s_and_b32 s40, s67, 0xffff0000
	v_pk_fma_f32 v[158:159], v[24:25], s[2:3], v[158:159] op_sel_hi:[1,0,1]
	v_pk_add_f32 v[156:157], v[156:157], v[160:161]
	s_lshl_b32 s2, s67, 16
	v_pk_mul_f32 v[160:161], v[38:39], s[40:41] op_sel_hi:[1,0]
	v_pk_add_f32 v[154:155], v[154:155], v[158:159]
	v_pk_mul_f32 v[158:159], v[40:41], s[40:41] op_sel_hi:[1,0]
	v_pk_fma_f32 v[160:161], v[34:35], s[2:3], v[160:161] op_sel_hi:[1,0,1]
	s_and_b32 s40, s73, 0xffff0000
	v_pk_fma_f32 v[158:159], v[36:37], s[2:3], v[158:159] op_sel_hi:[1,0,1]
	v_pk_add_f32 v[156:157], v[156:157], v[160:161]
	s_lshl_b32 s2, s73, 16
	v_pk_mul_f32 v[160:161], v[46:47], s[40:41] op_sel_hi:[1,0]
	v_pk_add_f32 v[154:155], v[154:155], v[158:159]
	v_pk_mul_f32 v[158:159], v[48:49], s[40:41] op_sel_hi:[1,0]
	v_pk_fma_f32 v[160:161], v[42:43], s[2:3], v[160:161] op_sel_hi:[1,0,1]
	s_and_b32 s40, s74, 0xffff0000
	v_pk_fma_f32 v[158:159], v[44:45], s[2:3], v[158:159] op_sel_hi:[1,0,1]
	v_pk_add_f32 v[156:157], v[156:157], v[160:161]
	s_lshl_b32 s2, s74, 16
	v_pk_mul_f32 v[160:161], v[54:55], s[40:41] op_sel_hi:[1,0]
	s_and_b32 s58, s75, 0xffff0000
	v_pk_fma_f32 v[160:161], v[50:51], s[2:3], v[160:161] op_sel_hi:[1,0,1]
	v_pk_add_f32 v[154:155], v[154:155], v[158:159]
	v_pk_mul_f32 v[158:159], v[56:57], s[40:41] op_sel_hi:[1,0]
	v_pk_add_f32 v[156:157], v[156:157], v[160:161]
	s_lshl_b32 s40, s75, 16
	v_pk_mul_f32 v[160:161], v[62:63], s[58:59] op_sel_hi:[1,0]
	v_pk_fma_f32 v[158:159], v[52:53], s[2:3], v[158:159] op_sel_hi:[1,0,1]
	v_pk_fma_f32 v[160:161], v[58:59], s[40:41], v[160:161] op_sel_hi:[1,0,1]
	v_pk_add_f32 v[154:155], v[154:155], v[158:159]
	v_pk_add_f32 v[156:157], v[156:157], v[160:161]
	v_pk_mul_f32 v[158:159], v[64:65], s[58:59] op_sel_hi:[1,0]
	v_mul_f32_e64 v160, |v156|, s53
	v_exp_f32_e32 v160, v160
	v_pk_fma_f32 v[158:159], v[60:61], s[40:41], v[158:159] op_sel_hi:[1,0,1]
	v_min_f32_e32 v156, 0, v156
	v_pk_add_f32 v[154:155], v[154:155], v[158:159]
	v_add_f32_e32 v160, 1.0, v160
	v_mul_f32_e64 v159, |v157|, s53
	v_exp_f32_e32 v159, v159
	v_log_f32_e32 v160, v160
	v_min_f32_e32 v157, 0, v157
	v_readlane_b32 s58, v72, 8
	v_readlane_b32 s66, v73, 8
	v_readlane_b32 s67, v70, 9
	v_readlane_b32 s73, v71, 9
	v_fma_f32 v156, -v160, s69, v156
	v_add_f32_e32 v158, 1.0, v159
	v_readlane_b32 s74, v72, 9
	v_readlane_b32 s75, v73, 9
	v_log_f32_e32 v158, v158
	v_mul_f32_e32 v156, 0x3d800000, v156
	v_max_f32_e32 v156, -1.0, v156
	v_mul_f32_e32 v151, 0x3d800000, v151
	v_max_f32_e32 v151, -1.0, v151
	v_mul_f32_e64 v159, |v154|, s53
	v_exp_f32_e32 v159, v159
	v_fma_f32 v157, -v158, s69, v157
	v_min_f32_e32 v154, 0, v154
	v_add_f32_e32 v158, 1.0, v159
	v_mul_f32_e32 v157, 0x3d800000, v157
	v_max_f32_e32 v157, -1.0, v157
	v_log_f32_e32 v158, v158
	v_mul_f32_e64 v159, |v155|, s53
	v_exp_f32_e32 v159, v159
	v_fma_f32 v154, -v158, s69, v154
	v_min_f32_e32 v155, 0, v155
	v_add_f32_e32 v158, 1.0, v159
	v_mul_f32_e32 v154, 0x3d800000, v154
	v_max_f32_e32 v154, -1.0, v154
	v_log_f32_e32 v158, v158
	v_readlane_b32 s40, v70, 8
	v_readlane_b32 s41, v71, 8
	s_lshl_b32 s2, s40, 16
	s_and_b32 s40, s40, 0xffff0000
	v_fma_f32 v155, -v158, s69, v155
	v_pk_mul_f32 v[158:159], v[4:5], s[40:41] op_sel_hi:[1,0]
	v_pk_mul_f32 v[160:161], v[2:3], s[40:41] op_sel_hi:[1,0]
	s_and_b32 s40, s41, 0xffff0000
	v_pk_fma_f32 v[158:159], v[28:29], s[2:3], v[158:159] op_sel_hi:[1,0,1]
	v_pk_fma_f32 v[160:161], v[26:27], s[2:3], v[160:161] op_sel_hi:[1,0,1]
	s_lshl_b32 s2, s41, 16
	v_pk_mul_f32 v[164:165], v[10:11], s[40:41] op_sel_hi:[1,0]
	v_pk_add_f32 v[160:161], v[66:67], v[160:161]
	v_pk_mul_f32 v[162:163], v[12:13], s[40:41] op_sel_hi:[1,0]
	v_pk_fma_f32 v[164:165], v[6:7], s[2:3], v[164:165] op_sel_hi:[1,0,1]
	s_and_b32 s40, s58, 0xffff0000
	v_pk_add_f32 v[158:159], v[68:69], v[158:159]
	v_pk_fma_f32 v[162:163], v[8:9], s[2:3], v[162:163] op_sel_hi:[1,0,1]
	v_pk_add_f32 v[160:161], v[160:161], v[164:165]
	s_lshl_b32 s2, s58, 16
	v_pk_mul_f32 v[164:165], v[18:19], s[40:41] op_sel_hi:[1,0]
	v_pk_add_f32 v[158:159], v[158:159], v[162:163]
	v_pk_mul_f32 v[162:163], v[20:21], s[40:41] op_sel_hi:[1,0]
	v_pk_fma_f32 v[164:165], v[14:15], s[2:3], v[164:165] op_sel_hi:[1,0,1]
	s_and_b32 s40, s66, 0xffff0000
	v_pk_fma_f32 v[162:163], v[16:17], s[2:3], v[162:163] op_sel_hi:[1,0,1]
	v_pk_add_f32 v[160:161], v[160:161], v[164:165]
	s_lshl_b32 s2, s66, 16
	v_pk_mul_f32 v[164:165], v[30:31], s[40:41] op_sel_hi:[1,0]
	v_pk_add_f32 v[158:159], v[158:159], v[162:163]
	v_pk_mul_f32 v[162:163], v[32:33], s[40:41] op_sel_hi:[1,0]
	v_pk_fma_f32 v[164:165], v[22:23], s[2:3], v[164:165] op_sel_hi:[1,0,1]
	s_and_b32 s40, s67, 0xffff0000
	v_pk_fma_f32 v[162:163], v[24:25], s[2:3], v[162:163] op_sel_hi:[1,0,1]
	v_pk_add_f32 v[160:161], v[160:161], v[164:165]
	s_lshl_b32 s2, s67, 16
	v_pk_mul_f32 v[164:165], v[38:39], s[40:41] op_sel_hi:[1,0]
	v_pk_add_f32 v[158:159], v[158:159], v[162:163]
	v_pk_mul_f32 v[162:163], v[40:41], s[40:41] op_sel_hi:[1,0]
	v_pk_fma_f32 v[164:165], v[34:35], s[2:3], v[164:165] op_sel_hi:[1,0,1]
	s_and_b32 s40, s73, 0xffff0000
	v_pk_fma_f32 v[162:163], v[36:37], s[2:3], v[162:163] op_sel_hi:[1,0,1]
	v_pk_add_f32 v[160:161], v[160:161], v[164:165]
	s_lshl_b32 s2, s73, 16
	v_pk_mul_f32 v[164:165], v[46:47], s[40:41] op_sel_hi:[1,0]
	v_pk_add_f32 v[158:159], v[158:159], v[162:163]
	v_pk_mul_f32 v[162:163], v[48:49], s[40:41] op_sel_hi:[1,0]
	v_pk_fma_f32 v[164:165], v[42:43], s[2:3], v[164:165] op_sel_hi:[1,0,1]
	s_and_b32 s40, s74, 0xffff0000
	v_pk_fma_f32 v[162:163], v[44:45], s[2:3], v[162:163] op_sel_hi:[1,0,1]
	v_pk_add_f32 v[160:161], v[160:161], v[164:165]
	s_lshl_b32 s2, s74, 16
	v_pk_mul_f32 v[164:165], v[54:55], s[40:41] op_sel_hi:[1,0]
	s_and_b32 s58, s75, 0xffff0000
	v_pk_fma_f32 v[164:165], v[50:51], s[2:3], v[164:165] op_sel_hi:[1,0,1]
	v_pk_add_f32 v[158:159], v[158:159], v[162:163]
	v_pk_mul_f32 v[162:163], v[56:57], s[40:41] op_sel_hi:[1,0]
	v_pk_add_f32 v[160:161], v[160:161], v[164:165]
	s_lshl_b32 s40, s75, 16
	v_pk_mul_f32 v[164:165], v[62:63], s[58:59] op_sel_hi:[1,0]
	v_pk_fma_f32 v[162:163], v[52:53], s[2:3], v[162:163] op_sel_hi:[1,0,1]
	v_pk_fma_f32 v[164:165], v[58:59], s[40:41], v[164:165] op_sel_hi:[1,0,1]
	v_pk_add_f32 v[158:159], v[158:159], v[162:163]
	v_pk_add_f32 v[160:161], v[160:161], v[164:165]
	v_pk_mul_f32 v[162:163], v[64:65], s[58:59] op_sel_hi:[1,0]
	v_mul_f32_e64 v164, |v160|, s53
	v_exp_f32_e32 v164, v164
	v_pk_fma_f32 v[162:163], v[60:61], s[40:41], v[162:163] op_sel_hi:[1,0,1]
	v_min_f32_e32 v160, 0, v160
	v_pk_add_f32 v[158:159], v[158:159], v[162:163]
	v_add_f32_e32 v164, 1.0, v164
	v_mul_f32_e64 v163, |v161|, s53
	v_exp_f32_e32 v163, v163
	v_log_f32_e32 v164, v164
	v_min_f32_e32 v161, 0, v161
	v_readlane_b32 s58, v72, 10
	v_readlane_b32 s66, v73, 10
	v_readlane_b32 s67, v70, 11
	v_readlane_b32 s73, v71, 11
	v_fma_f32 v160, -v164, s69, v160
	v_add_f32_e32 v162, 1.0, v163
	v_readlane_b32 s74, v72, 11
	v_readlane_b32 s75, v73, 11
	v_log_f32_e32 v162, v162
	v_mul_f32_e32 v160, 0x3d800000, v160
	v_max_f32_e32 v160, -1.0, v160
	v_mul_f32_e32 v155, 0x3d800000, v155
	v_max_f32_e32 v155, -1.0, v155
	v_mul_f32_e64 v163, |v158|, s53
	v_exp_f32_e32 v163, v163
	v_fma_f32 v161, -v162, s69, v161
	v_min_f32_e32 v158, 0, v158
	v_add_f32_e32 v162, 1.0, v163
	v_mul_f32_e32 v161, 0x3d800000, v161
	v_max_f32_e32 v161, -1.0, v161
	v_log_f32_e32 v162, v162
	v_mul_f32_e64 v163, |v159|, s53
	v_exp_f32_e32 v163, v163
	v_fma_f32 v158, -v162, s69, v158
	v_min_f32_e32 v159, 0, v159
	v_add_f32_e32 v162, 1.0, v163
	v_mul_f32_e32 v158, 0x3d800000, v158
	v_max_f32_e32 v158, -1.0, v158
	v_log_f32_e32 v162, v162
	v_readlane_b32 s40, v70, 10
	v_readlane_b32 s41, v71, 10
	s_lshl_b32 s2, s40, 16
	s_and_b32 s40, s40, 0xffff0000
	v_fma_f32 v159, -v162, s69, v159
	v_pk_mul_f32 v[162:163], v[4:5], s[40:41] op_sel_hi:[1,0]
	v_pk_mul_f32 v[164:165], v[2:3], s[40:41] op_sel_hi:[1,0]
	s_and_b32 s40, s41, 0xffff0000
	v_pk_fma_f32 v[162:163], v[28:29], s[2:3], v[162:163] op_sel_hi:[1,0,1]
	v_pk_fma_f32 v[164:165], v[26:27], s[2:3], v[164:165] op_sel_hi:[1,0,1]
	s_lshl_b32 s2, s41, 16
	v_pk_mul_f32 v[168:169], v[10:11], s[40:41] op_sel_hi:[1,0]
	v_pk_add_f32 v[164:165], v[66:67], v[164:165]
	v_pk_mul_f32 v[166:167], v[12:13], s[40:41] op_sel_hi:[1,0]
	v_pk_fma_f32 v[168:169], v[6:7], s[2:3], v[168:169] op_sel_hi:[1,0,1]
	s_and_b32 s40, s58, 0xffff0000
	v_pk_add_f32 v[162:163], v[68:69], v[162:163]
	v_pk_fma_f32 v[166:167], v[8:9], s[2:3], v[166:167] op_sel_hi:[1,0,1]
	v_pk_add_f32 v[164:165], v[164:165], v[168:169]
	s_lshl_b32 s2, s58, 16
	v_pk_mul_f32 v[168:169], v[18:19], s[40:41] op_sel_hi:[1,0]
	v_pk_add_f32 v[162:163], v[162:163], v[166:167]
	v_pk_mul_f32 v[166:167], v[20:21], s[40:41] op_sel_hi:[1,0]
	v_pk_fma_f32 v[168:169], v[14:15], s[2:3], v[168:169] op_sel_hi:[1,0,1]
	s_and_b32 s40, s66, 0xffff0000
	v_pk_fma_f32 v[166:167], v[16:17], s[2:3], v[166:167] op_sel_hi:[1,0,1]
	v_pk_add_f32 v[164:165], v[164:165], v[168:169]
	s_lshl_b32 s2, s66, 16
	v_pk_mul_f32 v[168:169], v[30:31], s[40:41] op_sel_hi:[1,0]
	v_pk_add_f32 v[162:163], v[162:163], v[166:167]
	v_pk_mul_f32 v[166:167], v[32:33], s[40:41] op_sel_hi:[1,0]
	v_pk_fma_f32 v[168:169], v[22:23], s[2:3], v[168:169] op_sel_hi:[1,0,1]
	s_and_b32 s40, s67, 0xffff0000
	v_pk_fma_f32 v[166:167], v[24:25], s[2:3], v[166:167] op_sel_hi:[1,0,1]
	v_pk_add_f32 v[164:165], v[164:165], v[168:169]
	s_lshl_b32 s2, s67, 16
	v_pk_mul_f32 v[168:169], v[38:39], s[40:41] op_sel_hi:[1,0]
	v_pk_add_f32 v[162:163], v[162:163], v[166:167]
	v_pk_mul_f32 v[166:167], v[40:41], s[40:41] op_sel_hi:[1,0]
	v_pk_fma_f32 v[168:169], v[34:35], s[2:3], v[168:169] op_sel_hi:[1,0,1]
	s_and_b32 s40, s73, 0xffff0000
	v_pk_fma_f32 v[166:167], v[36:37], s[2:3], v[166:167] op_sel_hi:[1,0,1]
	v_pk_add_f32 v[164:165], v[164:165], v[168:169]
	s_lshl_b32 s2, s73, 16
	v_pk_mul_f32 v[168:169], v[46:47], s[40:41] op_sel_hi:[1,0]
	v_pk_add_f32 v[162:163], v[162:163], v[166:167]
	v_pk_mul_f32 v[166:167], v[48:49], s[40:41] op_sel_hi:[1,0]
	v_pk_fma_f32 v[168:169], v[42:43], s[2:3], v[168:169] op_sel_hi:[1,0,1]
	s_and_b32 s40, s74, 0xffff0000
	v_pk_fma_f32 v[166:167], v[44:45], s[2:3], v[166:167] op_sel_hi:[1,0,1]
	v_pk_add_f32 v[164:165], v[164:165], v[168:169]
	s_lshl_b32 s2, s74, 16
	v_pk_mul_f32 v[168:169], v[54:55], s[40:41] op_sel_hi:[1,0]
	s_and_b32 s58, s75, 0xffff0000
	v_pk_fma_f32 v[168:169], v[50:51], s[2:3], v[168:169] op_sel_hi:[1,0,1]
	v_pk_add_f32 v[162:163], v[162:163], v[166:167]
	v_pk_mul_f32 v[166:167], v[56:57], s[40:41] op_sel_hi:[1,0]
	v_pk_add_f32 v[164:165], v[164:165], v[168:169]
	s_lshl_b32 s40, s75, 16
	v_pk_mul_f32 v[168:169], v[62:63], s[58:59] op_sel_hi:[1,0]
	v_pk_fma_f32 v[166:167], v[52:53], s[2:3], v[166:167] op_sel_hi:[1,0,1]
	v_pk_fma_f32 v[168:169], v[58:59], s[40:41], v[168:169] op_sel_hi:[1,0,1]
	v_pk_add_f32 v[162:163], v[162:163], v[166:167]
	v_pk_add_f32 v[164:165], v[164:165], v[168:169]
	v_pk_mul_f32 v[166:167], v[64:65], s[58:59] op_sel_hi:[1,0]
	v_mul_f32_e64 v168, |v164|, s53
	v_exp_f32_e32 v168, v168
	v_pk_fma_f32 v[166:167], v[60:61], s[40:41], v[166:167] op_sel_hi:[1,0,1]
	v_min_f32_e32 v164, 0, v164
	v_pk_add_f32 v[162:163], v[162:163], v[166:167]
	v_add_f32_e32 v168, 1.0, v168
	v_mul_f32_e64 v167, |v165|, s53
	v_exp_f32_e32 v167, v167
	v_log_f32_e32 v168, v168
	v_readlane_b32 s58, v72, 12
	v_readlane_b32 s66, v73, 12
	v_readlane_b32 s67, v70, 13
	v_readlane_b32 s73, v71, 13
	v_readlane_b32 s74, v72, 13
	v_fma_f32 v164, -v168, s69, v164
	v_add_f32_e32 v166, 1.0, v167
	v_mul_f32_e32 v164, 0x3d800000, v164
	v_readlane_b32 s75, v73, 13
	v_log_f32_e32 v167, v166
	v_max_f32_e32 v166, -1.0, v164
	v_min_f32_e32 v164, 0, v165
	v_mul_f32_e32 v165, 0x3f317217, v167
	v_mul_f32_e32 v159, 0x3d800000, v159
	v_max_f32_e32 v159, -1.0, v159
	v_mul_f32_e64 v167, |v162|, s53
	v_exp_f32_e32 v167, v167
	v_sub_f32_e32 v164, v164, v165
	v_mul_f32_e32 v164, 0x3d800000, v164
	v_add_f32_e32 v165, 1.0, v167
	v_min_f32_e32 v162, 0, v162
	v_log_f32_e32 v165, v165
	v_max_f32_e32 v167, -1.0, v164
	v_mul_f32_e32 v164, 0x3f317217, v165
	v_mul_f32_e64 v165, |v163|, s53
	v_exp_f32_e32 v165, v165
	v_sub_f32_e32 v162, v162, v164
	v_mul_f32_e32 v162, 0x3d800000, v162
	v_add_f32_e32 v164, 1.0, v165
	v_log_f32_e32 v165, v164
	v_max_f32_e32 v164, -1.0, v162
	v_min_f32_e32 v162, 0, v163
	v_fma_f32 v162, -v165, s69, v162
	v_readlane_b32 s40, v70, 12
	v_mul_f32_e32 v162, 0x3d800000, v162
	v_readlane_b32 s41, v71, 12
	s_lshl_b32 s2, s40, 16
	s_and_b32 s40, s40, 0xffff0000
	v_max_f32_e32 v165, -1.0, v162
	v_pk_mul_f32 v[162:163], v[4:5], s[40:41] op_sel_hi:[1,0]
	v_pk_mul_f32 v[168:169], v[2:3], s[40:41] op_sel_hi:[1,0]
	s_and_b32 s40, s41, 0xffff0000
	v_pk_fma_f32 v[162:163], v[28:29], s[2:3], v[162:163] op_sel_hi:[1,0,1]
	v_pk_fma_f32 v[168:169], v[26:27], s[2:3], v[168:169] op_sel_hi:[1,0,1]
	s_lshl_b32 s2, s41, 16
	v_pk_mul_f32 v[172:173], v[10:11], s[40:41] op_sel_hi:[1,0]
	v_pk_add_f32 v[168:169], v[66:67], v[168:169]
	v_pk_mul_f32 v[170:171], v[12:13], s[40:41] op_sel_hi:[1,0]
	v_pk_fma_f32 v[172:173], v[6:7], s[2:3], v[172:173] op_sel_hi:[1,0,1]
	s_and_b32 s40, s58, 0xffff0000
	v_pk_add_f32 v[162:163], v[68:69], v[162:163]
	v_pk_fma_f32 v[170:171], v[8:9], s[2:3], v[170:171] op_sel_hi:[1,0,1]
	v_pk_add_f32 v[168:169], v[168:169], v[172:173]
	s_lshl_b32 s2, s58, 16
	v_pk_mul_f32 v[172:173], v[18:19], s[40:41] op_sel_hi:[1,0]
	v_pk_add_f32 v[162:163], v[162:163], v[170:171]
	v_pk_mul_f32 v[170:171], v[20:21], s[40:41] op_sel_hi:[1,0]
	v_pk_fma_f32 v[172:173], v[14:15], s[2:3], v[172:173] op_sel_hi:[1,0,1]
	s_and_b32 s40, s66, 0xffff0000
	v_pk_fma_f32 v[170:171], v[16:17], s[2:3], v[170:171] op_sel_hi:[1,0,1]
	v_pk_add_f32 v[168:169], v[168:169], v[172:173]
	s_lshl_b32 s2, s66, 16
	v_pk_mul_f32 v[172:173], v[30:31], s[40:41] op_sel_hi:[1,0]
	v_pk_add_f32 v[162:163], v[162:163], v[170:171]
	v_pk_mul_f32 v[170:171], v[32:33], s[40:41] op_sel_hi:[1,0]
	v_pk_fma_f32 v[172:173], v[22:23], s[2:3], v[172:173] op_sel_hi:[1,0,1]
	s_and_b32 s40, s67, 0xffff0000
	v_pk_fma_f32 v[170:171], v[24:25], s[2:3], v[170:171] op_sel_hi:[1,0,1]
	v_pk_add_f32 v[168:169], v[168:169], v[172:173]
	s_lshl_b32 s2, s67, 16
	v_pk_mul_f32 v[172:173], v[38:39], s[40:41] op_sel_hi:[1,0]
	v_pk_add_f32 v[162:163], v[162:163], v[170:171]
	v_pk_mul_f32 v[170:171], v[40:41], s[40:41] op_sel_hi:[1,0]
	v_pk_fma_f32 v[172:173], v[34:35], s[2:3], v[172:173] op_sel_hi:[1,0,1]
	s_and_b32 s40, s73, 0xffff0000
	v_pk_fma_f32 v[170:171], v[36:37], s[2:3], v[170:171] op_sel_hi:[1,0,1]
	v_pk_add_f32 v[168:169], v[168:169], v[172:173]
	s_lshl_b32 s2, s73, 16
	v_pk_mul_f32 v[172:173], v[46:47], s[40:41] op_sel_hi:[1,0]
	v_pk_add_f32 v[162:163], v[162:163], v[170:171]
	v_pk_mul_f32 v[170:171], v[48:49], s[40:41] op_sel_hi:[1,0]
	v_pk_fma_f32 v[172:173], v[42:43], s[2:3], v[172:173] op_sel_hi:[1,0,1]
	s_and_b32 s40, s74, 0xffff0000
	v_pk_fma_f32 v[170:171], v[44:45], s[2:3], v[170:171] op_sel_hi:[1,0,1]
	v_pk_add_f32 v[168:169], v[168:169], v[172:173]
	s_lshl_b32 s2, s74, 16
	v_pk_mul_f32 v[172:173], v[54:55], s[40:41] op_sel_hi:[1,0]
	s_and_b32 s58, s75, 0xffff0000
	v_pk_fma_f32 v[172:173], v[50:51], s[2:3], v[172:173] op_sel_hi:[1,0,1]
	v_pk_add_f32 v[162:163], v[162:163], v[170:171]
	v_pk_mul_f32 v[170:171], v[56:57], s[40:41] op_sel_hi:[1,0]
	v_pk_add_f32 v[168:169], v[168:169], v[172:173]
	s_lshl_b32 s40, s75, 16
	v_pk_mul_f32 v[172:173], v[62:63], s[58:59] op_sel_hi:[1,0]
	v_pk_fma_f32 v[170:171], v[52:53], s[2:3], v[170:171] op_sel_hi:[1,0,1]
	v_pk_fma_f32 v[172:173], v[58:59], s[40:41], v[172:173] op_sel_hi:[1,0,1]
	v_pk_add_f32 v[162:163], v[162:163], v[170:171]
	v_pk_add_f32 v[168:169], v[168:169], v[172:173]
	v_pk_mul_f32 v[170:171], v[64:65], s[58:59] op_sel_hi:[1,0]
	v_mul_f32_e64 v172, |v168|, s53
	v_exp_f32_e32 v172, v172
	v_pk_fma_f32 v[170:171], v[60:61], s[40:41], v[170:171] op_sel_hi:[1,0,1]
	v_min_f32_e32 v168, 0, v168
	v_pk_add_f32 v[162:163], v[162:163], v[170:171]
	v_add_f32_e32 v172, 1.0, v172
	v_mul_f32_e64 v171, |v169|, s53
	v_exp_f32_e32 v171, v171
	v_log_f32_e32 v172, v172
	v_readlane_b32 s58, v72, 14
	v_readlane_b32 s66, v73, 14
	v_readlane_b32 s67, v70, 15
	v_readlane_b32 s73, v71, 15
	v_readlane_b32 s74, v72, 15
	v_fma_f32 v168, -v172, s69, v168
	v_add_f32_e32 v170, 1.0, v171
	v_mul_f32_e32 v168, 0x3d800000, v168
	v_readlane_b32 s75, v73, 15
	v_log_f32_e32 v171, v170
	v_max_f32_e32 v170, -1.0, v168
	v_min_f32_e32 v168, 0, v169
	v_mul_f32_e32 v169, 0x3f317217, v171
	v_mul_f32_e64 v171, |v162|, s53
	v_exp_f32_e32 v171, v171
	v_sub_f32_e32 v168, v168, v169
	v_mul_f32_e32 v168, 0x3d800000, v168
	v_add_f32_e32 v169, 1.0, v171
	v_min_f32_e32 v162, 0, v162
	v_log_f32_e32 v169, v169
	v_max_f32_e32 v171, -1.0, v168
	v_mul_f32_e32 v168, 0x3f317217, v169
	v_mul_f32_e64 v169, |v163|, s53
	v_exp_f32_e32 v169, v169
	v_sub_f32_e32 v162, v162, v168
	v_mul_f32_e32 v162, 0x3d800000, v162
	v_add_f32_e32 v168, 1.0, v169
	v_max_f32_e32 v178, -1.0, v162
	v_min_f32_e32 v162, 0, v163
	v_log_f32_e32 v168, v168
	s_nop 0
	v_fma_f32 v162, -v168, s69, v162
	v_readlane_b32 s40, v70, 14
	v_mul_f32_e32 v162, 0x3d800000, v162
	v_readlane_b32 s41, v71, 14
	s_lshl_b32 s2, s40, 16
	s_and_b32 s40, s40, 0xffff0000
	v_max_f32_e32 v179, -1.0, v162
	v_pk_mul_f32 v[162:163], v[4:5], s[40:41] op_sel_hi:[1,0]
	v_pk_mul_f32 v[168:169], v[2:3], s[40:41] op_sel_hi:[1,0]
	s_and_b32 s40, s41, 0xffff0000
	v_pk_fma_f32 v[162:163], v[28:29], s[2:3], v[162:163] op_sel_hi:[1,0,1]
	v_pk_fma_f32 v[168:169], v[26:27], s[2:3], v[168:169] op_sel_hi:[1,0,1]
	s_lshl_b32 s2, s41, 16
	v_pk_mul_f32 v[174:175], v[10:11], s[40:41] op_sel_hi:[1,0]
	v_pk_add_f32 v[168:169], v[66:67], v[168:169]
	v_pk_mul_f32 v[172:173], v[12:13], s[40:41] op_sel_hi:[1,0]
	v_pk_fma_f32 v[174:175], v[6:7], s[2:3], v[174:175] op_sel_hi:[1,0,1]
	s_and_b32 s40, s58, 0xffff0000
	v_pk_add_f32 v[162:163], v[68:69], v[162:163]
	v_pk_fma_f32 v[172:173], v[8:9], s[2:3], v[172:173] op_sel_hi:[1,0,1]
	v_pk_add_f32 v[168:169], v[168:169], v[174:175]
	s_lshl_b32 s2, s58, 16
	v_pk_mul_f32 v[174:175], v[18:19], s[40:41] op_sel_hi:[1,0]
	v_pk_add_f32 v[162:163], v[162:163], v[172:173]
	v_pk_mul_f32 v[172:173], v[20:21], s[40:41] op_sel_hi:[1,0]
	v_pk_fma_f32 v[174:175], v[14:15], s[2:3], v[174:175] op_sel_hi:[1,0,1]
	s_and_b32 s40, s66, 0xffff0000
	v_pk_fma_f32 v[172:173], v[16:17], s[2:3], v[172:173] op_sel_hi:[1,0,1]
	v_pk_add_f32 v[168:169], v[168:169], v[174:175]
	s_lshl_b32 s2, s66, 16
	v_pk_mul_f32 v[174:175], v[30:31], s[40:41] op_sel_hi:[1,0]
	v_pk_add_f32 v[162:163], v[162:163], v[172:173]
	v_pk_mul_f32 v[172:173], v[32:33], s[40:41] op_sel_hi:[1,0]
	v_pk_fma_f32 v[174:175], v[22:23], s[2:3], v[174:175] op_sel_hi:[1,0,1]
	s_and_b32 s40, s67, 0xffff0000
	v_pk_fma_f32 v[172:173], v[24:25], s[2:3], v[172:173] op_sel_hi:[1,0,1]
	v_pk_add_f32 v[168:169], v[168:169], v[174:175]
	s_lshl_b32 s2, s67, 16
	v_pk_mul_f32 v[174:175], v[38:39], s[40:41] op_sel_hi:[1,0]
	v_pk_add_f32 v[162:163], v[162:163], v[172:173]
	v_pk_mul_f32 v[172:173], v[40:41], s[40:41] op_sel_hi:[1,0]
	v_pk_fma_f32 v[174:175], v[34:35], s[2:3], v[174:175] op_sel_hi:[1,0,1]
	s_and_b32 s40, s73, 0xffff0000
	v_pk_fma_f32 v[172:173], v[36:37], s[2:3], v[172:173] op_sel_hi:[1,0,1]
	v_pk_add_f32 v[168:169], v[168:169], v[174:175]
	s_lshl_b32 s2, s73, 16
	v_pk_mul_f32 v[174:175], v[46:47], s[40:41] op_sel_hi:[1,0]
	v_pk_add_f32 v[162:163], v[162:163], v[172:173]
	v_pk_mul_f32 v[172:173], v[48:49], s[40:41] op_sel_hi:[1,0]
	v_pk_fma_f32 v[174:175], v[42:43], s[2:3], v[174:175] op_sel_hi:[1,0,1]
	s_and_b32 s40, s74, 0xffff0000
	v_pk_fma_f32 v[172:173], v[44:45], s[2:3], v[172:173] op_sel_hi:[1,0,1]
	v_pk_add_f32 v[168:169], v[168:169], v[174:175]
	s_lshl_b32 s2, s74, 16
	v_pk_mul_f32 v[174:175], v[54:55], s[40:41] op_sel_hi:[1,0]
	s_and_b32 s58, s75, 0xffff0000
	v_pk_fma_f32 v[174:175], v[50:51], s[2:3], v[174:175] op_sel_hi:[1,0,1]
	v_pk_add_f32 v[162:163], v[162:163], v[172:173]
	v_pk_mul_f32 v[172:173], v[56:57], s[40:41] op_sel_hi:[1,0]
	v_pk_add_f32 v[168:169], v[168:169], v[174:175]
	s_lshl_b32 s40, s75, 16
	v_pk_mul_f32 v[174:175], v[62:63], s[58:59] op_sel_hi:[1,0]
	v_pk_fma_f32 v[172:173], v[52:53], s[2:3], v[172:173] op_sel_hi:[1,0,1]
	v_pk_fma_f32 v[174:175], v[58:59], s[40:41], v[174:175] op_sel_hi:[1,0,1]
	v_pk_add_f32 v[162:163], v[162:163], v[172:173]
	v_pk_add_f32 v[168:169], v[168:169], v[174:175]
	v_pk_mul_f32 v[172:173], v[64:65], s[58:59] op_sel_hi:[1,0]
	v_mul_f32_e64 v174, |v168|, s53
	v_exp_f32_e32 v174, v174
	v_pk_fma_f32 v[172:173], v[60:61], s[40:41], v[172:173] op_sel_hi:[1,0,1]
	v_add_f32_e32 v174, 1.0, v174
	v_log_f32_e32 v176, v174
	v_pk_add_f32 v[174:175], v[162:163], v[172:173]
	v_min_f32_e32 v162, 0, v168
	v_mul_f32_e64 v168, |v169|, s53
	v_exp_f32_e32 v168, v168
	v_fma_f32 v162, -v176, s69, v162
	v_add_f32_e32 v163, 1.0, v168
	v_pk_add_f32 v[176:177], v[74:75], 0 op_sel_hi:[1,0]
	v_mul_f32_e64 v74, |v174|, s53
	v_log_f32_e32 v163, v163
	v_exp_f32_e32 v74, v74
	v_mul_f32_e32 v162, 0x3d800000, v162
	v_max_f32_e32 v186, -1.0, v162
	v_add_f32_e32 v74, 1.0, v74
	v_min_f32_e32 v162, 0, v169
	v_fma_f32 v162, -v163, s69, v162
	v_pk_add_f32 v[172:173], v[176:177], v[80:81]
	v_log_f32_e32 v80, v74
	v_mul_f32_e32 v162, 0x3d800000, v162
	v_pk_add_f32 v[168:169], v[172:173], v[152:153]
	v_max_f32_e32 v187, -1.0, v162
	v_pk_add_f32 v[162:163], v[168:169], v[156:157]
	v_pk_add_f32 v[160:161], v[162:163], v[160:161]
	v_min_f32_e32 v81, 0, v174
	v_pk_add_f32 v[156:157], v[160:161], v[166:167]
	v_mul_f32_e64 v166, |v175|, s53
	v_exp_f32_e32 v166, v166
	v_fma_f32 v80, -v80, s69, v81
	v_add_f32_e32 v81, 1.0, v166
	v_pk_add_f32 v[152:153], v[156:157], v[170:171]
	v_mul_f32_e32 v80, 0x3d800000, v80
	v_log_f32_e32 v81, v81
	v_min_f32_e32 v166, 0, v175
	v_pk_add_f32 v[174:175], v[190:191], v[78:79]
	v_max_f32_e32 v80, -1.0, v80
	v_pk_add_f32 v[170:171], v[174:175], v[150:151]
	v_pk_add_f32 v[74:75], v[152:153], v[186:187]
	v_fma_f32 v81, -v81, s69, v166
	v_pk_add_f32 v[166:167], v[170:171], v[154:155]
	v_mul_f32_e32 v81, 0x3d800000, v81
	v_pk_add_f32 v[158:159], v[166:167], v[158:159]
	v_max_f32_e32 v81, -1.0, v81
	v_pk_add_f32 v[154:155], v[158:159], v[164:165]
	s_ashr_i32 s41, s72, 31
	v_pk_add_f32 v[150:151], v[154:155], v[178:179]
	s_mov_b32 s40, s72
	v_pk_add_f32 v[76:77], v[150:151], v[80:81]
	ds_write_b128 v85, v[74:77]
	s_waitcnt lgkmcnt(0)
	s_barrier
	ds_read_b128 v[78:81], v97
	ds_read_b128 v[186:189], v97 offset:1024
	s_lshl_b64 s[66:67], s[40:41], 11
	s_andn2_b64 vcc, exec, s[60:61]
	s_waitcnt lgkmcnt(1)
	v_pk_add_f32 v[80:81], v[80:81], 0 op_sel_hi:[1,0]
	v_pk_add_f32 v[78:79], v[78:79], 0 op_sel_hi:[1,0]
	v_cndmask_b32_e64 v179, 0, v81, s[6:7]
	v_cndmask_b32_e64 v165, 0, v79, s[6:7]
	v_cndmask_b32_e64 v164, 0, v78, s[6:7]
	v_cndmask_b32_e64 v178, 0, v80, s[6:7]
	s_waitcnt lgkmcnt(0)
	v_pk_add_f32 v[192:193], v[80:81], v[188:189]
	v_pk_add_f32 v[194:195], v[78:79], v[186:187]
	ds_read_b128 v[78:81], v97 offset:2048
	v_pk_add_f32 v[186:187], v[186:187], v[164:165]
	v_pk_add_f32 v[188:189], v[188:189], v[178:179]
	v_cndmask_b32_e64 v165, v165, v187, s[8:9]
	v_cndmask_b32_e64 v164, v164, v186, s[8:9]
	v_cndmask_b32_e64 v179, v179, v189, s[8:9]
	v_cndmask_b32_e64 v178, v178, v188, s[8:9]
	ds_read_b128 v[186:189], v97 offset:3072
	s_waitcnt lgkmcnt(1)
	v_pk_add_f32 v[192:193], v[192:193], v[80:81]
	v_pk_add_f32 v[194:195], v[194:195], v[78:79]
	v_pk_add_f32 v[78:79], v[78:79], v[164:165]
	v_pk_add_f32 v[80:81], v[80:81], v[178:179]
	v_cndmask_b32_e64 v165, v165, v79, s[10:11]
	v_cndmask_b32_e64 v164, v164, v78, s[10:11]
	v_cndmask_b32_e64 v179, v179, v81, s[10:11]
	v_cndmask_b32_e64 v178, v178, v80, s[10:11]
	ds_read_b128 v[78:81], v97 offset:4096
	s_waitcnt lgkmcnt(1)
	v_pk_add_f32 v[192:193], v[192:193], v[188:189]
	v_pk_add_f32 v[194:195], v[194:195], v[186:187]
	v_pk_add_f32 v[186:187], v[186:187], v[164:165]
	v_pk_add_f32 v[188:189], v[188:189], v[178:179]
	v_cndmask_b32_e64 v165, v165, v187, s[12:13]
	v_cndmask_b32_e64 v164, v164, v186, s[12:13]
	v_cndmask_b32_e64 v179, v179, v189, s[12:13]
	v_cndmask_b32_e64 v178, v178, v188, s[12:13]
	ds_read_b128 v[186:189], v97 offset:5120
	s_waitcnt lgkmcnt(1)
	v_pk_add_f32 v[192:193], v[192:193], v[80:81]
	v_pk_add_f32 v[194:195], v[194:195], v[78:79]
	v_pk_add_f32 v[78:79], v[78:79], v[164:165]
	v_pk_add_f32 v[80:81], v[80:81], v[178:179]
	v_cndmask_b32_e64 v165, v165, v79, s[14:15]
	v_cndmask_b32_e64 v164, v164, v78, s[14:15]
	v_cndmask_b32_e64 v179, v179, v81, s[14:15]
	v_cndmask_b32_e64 v178, v178, v80, s[14:15]
	ds_read_b128 v[78:81], v97 offset:6144
	s_waitcnt lgkmcnt(1)
	v_pk_add_f32 v[192:193], v[192:193], v[188:189]
	v_pk_add_f32 v[194:195], v[194:195], v[186:187]
	v_pk_add_f32 v[186:187], v[186:187], v[164:165]
	v_pk_add_f32 v[188:189], v[188:189], v[178:179]
	v_cndmask_b32_e64 v165, v165, v187, s[16:17]
	v_cndmask_b32_e64 v164, v164, v186, s[16:17]
	v_cndmask_b32_e64 v179, v179, v189, s[16:17]
	v_cndmask_b32_e64 v178, v178, v188, s[16:17]
	ds_read_b128 v[186:189], v97 offset:7168
	s_waitcnt lgkmcnt(1)
	v_pk_add_f32 v[194:195], v[194:195], v[78:79]
	v_pk_add_f32 v[78:79], v[78:79], v[164:165]
	v_pk_add_f32 v[192:193], v[192:193], v[80:81]
	v_cndmask_b32_e64 v165, v165, v79, s[18:19]
	v_cndmask_b32_e64 v164, v164, v78, s[18:19]
	s_waitcnt lgkmcnt(0)
	v_pk_add_f32 v[78:79], v[194:195], v[186:187]
	v_pk_add_f32 v[186:187], v[186:187], v[164:165]
	v_pk_add_f32 v[80:81], v[80:81], v[178:179]
	v_cndmask_b32_e64 v186, v164, v186, s[20:21]
	v_add_f32_e32 v176, v176, v186
	v_mul_f32_e32 v195, 0x3fb8aa3b, v176
	v_exp_f32_e32 v195, v195
	v_mul_f32_e32 v176, 0xbfb8aa3b, v176
	v_exp_f32_e32 v176, v176
	s_waitcnt vmcnt(8)
	v_lshlrev_b32_e32 v164, 16, v126
	v_cndmask_b32_e64 v187, v165, v187, s[20:21]
	v_mul_f32_e32 v164, 0x3d800000, v164
	v_cndmask_b32_e64 v179, v179, v81, s[18:19]
	v_cndmask_b32_e64 v178, v178, v80, s[18:19]
	v_pk_add_f32 v[80:81], v[192:193], v[188:189]
	v_lshlrev_b32_e32 v192, 16, v104
	v_mul_f32_e32 v195, v164, v195
	v_add_f32_e32 v164, v177, v187
	v_mul_f32_e32 v192, v176, v192
	v_mul_f32_e32 v176, 0x3fb8aa3b, v164
	v_mul_f32_e32 v164, 0xbfb8aa3b, v164
	v_exp_f32_e32 v164, v164
	v_exp_f32_e32 v176, v176
	v_pk_add_f32 v[188:189], v[188:189], v[178:179]
	v_and_b32_e32 v165, 0xffff0000, v126
	v_cndmask_b32_e64 v178, v178, v188, s[20:21]
	v_and_b32_e32 v193, 0xffff0000, v104
	v_mul_f32_e32 v165, 0x3d800000, v165
	v_mul_f32_e32 v193, v164, v193
	v_add_f32_e32 v164, v190, v178
	v_mul_f32_e32 v176, v165, v176
	v_mul_f32_e32 v165, 0x3fb8aa3b, v164
	v_mul_f32_e32 v164, 0xbfb8aa3b, v164
	v_exp_f32_e32 v164, v164
	v_exp_f32_e32 v165, v165
	v_cndmask_b32_e64 v179, v179, v189, s[20:21]
	v_lshlrev_b32_e32 v188, 16, v127
	v_lshlrev_b32_e32 v194, 16, v105
	v_mul_f32_e32 v177, 0x3d800000, v188
	v_mul_f32_e32 v188, v164, v194
	v_add_f32_e32 v164, v191, v179
	v_mul_f32_e32 v177, v177, v165
	v_mul_f32_e32 v165, 0x3fb8aa3b, v164
	v_mul_f32_e32 v164, 0xbfb8aa3b, v164
	v_mul_f32_e32 v81, 0x3fb8aa3b, v81
	v_exp_f32_e32 v191, v165
	v_exp_f32_e32 v164, v164
	v_add_f32_e32 v172, v172, v186
	v_exp_f32_e32 v81, v81
	v_mul_f32_e32 v194, 0x3fb8aa3b, v172
	v_mul_f32_e32 v172, 0xbfb8aa3b, v172
	v_and_b32_e32 v189, 0xffff0000, v127
	v_exp_f32_e32 v172, v172
	v_mul_f32_e32 v189, 0x3d800000, v189
	v_mul_f32_e32 v189, v189, v191
	v_mul_f32_e32 v191, v164, v196
	v_cvt_pk_bf16_f32 v176, v195, v176
	v_cvt_pk_bf16_f32 v177, v177, v189
	v_mul_f32_e32 v164, v81, v191
	ds_write_b64 v101, v[176:177]
	v_cvt_pk_bf16_f32 v176, v192, v193
	v_cvt_pk_bf16_f32 v177, v188, v191
	s_waitcnt vmcnt(13)
	v_lshlrev_b32_e32 v191, 16, v108
	v_mul_f32_e32 v78, 0x3fb8aa3b, v78
	v_mul_f32_e32 v191, v172, v191
	v_add_f32_e32 v172, v173, v187
	v_exp_f32_e32 v78, v78
	v_mul_f32_e32 v173, 0x3fb8aa3b, v172
	v_mul_f32_e32 v172, 0xbfb8aa3b, v172
	v_exp_f32_e32 v173, v173
	v_exp_f32_e32 v172, v172
	ds_write_b64 v101, v[176:177] offset:33792
	s_waitcnt vmcnt(12)
	v_and_b32_e32 v177, 0xffff0000, v114
	v_mul_f32_e32 v80, 0x3fb8aa3b, v80
	v_mul_f32_e32 v197, v78, v192
	v_and_b32_e32 v192, 0xffff0000, v108
	v_mul_f32_e32 v177, 0x3d800000, v177
	v_mul_f32_e32 v79, 0x3fb8aa3b, v79
	v_exp_f32_e32 v80, v80
	v_mul_f32_e32 v173, v177, v173
	v_mul_f32_e32 v177, v172, v192
	v_add_f32_e32 v172, v174, v178
	v_exp_f32_e32 v79, v79
	v_mul_f32_e32 v174, 0x3fb8aa3b, v172
	v_mul_f32_e32 v172, 0xbfb8aa3b, v172
	v_exp_f32_e32 v174, v174
	v_exp_f32_e32 v172, v172
	v_mul_f32_e32 v165, v80, v188
	v_lshlrev_b32_e32 v188, 16, v115
	v_mul_f32_e32 v190, v79, v193
	v_lshlrev_b32_e32 v193, 16, v109
	v_mul_f32_e32 v188, 0x3d800000, v188
	v_mul_f32_e32 v174, v188, v174
	v_mul_f32_e32 v188, v172, v193
	v_add_f32_e32 v172, v175, v179
	v_mul_f32_e32 v175, 0x3fb8aa3b, v172
	v_mul_f32_e32 v172, 0xbfb8aa3b, v172
	v_exp_f32_e32 v194, v194
	v_exp_f32_e32 v175, v175
	v_exp_f32_e32 v172, v172
	v_lshlrev_b32_e32 v176, 16, v114
	v_and_b32_e32 v189, 0xffff0000, v115
	v_and_b32_e32 v195, 0xffff0000, v109
	v_mul_f32_e32 v176, 0x3d800000, v176
	v_mul_f32_e32 v189, 0x3d800000, v189
	v_mul_f32_e32 v176, v176, v194
	v_mul_f32_e32 v175, v189, v175
	v_mul_f32_e32 v189, v172, v195
	v_cvt_pk_bf16_f32 v172, v176, v173
	v_cvt_pk_bf16_f32 v173, v174, v175
	v_add_f32_e32 v168, v168, v186
	v_mul_f32_e32 v195, v81, v189
	ds_write_b64 v101, v[172:173] offset:528
	v_cvt_pk_bf16_f32 v172, v191, v177
	v_cvt_pk_bf16_f32 v173, v188, v189
	v_mul_f32_e32 v189, 0x3fb8aa3b, v168
	v_mul_f32_e32 v168, 0xbfb8aa3b, v168
	v_exp_f32_e32 v168, v168
	s_waitcnt vmcnt(10)
	v_lshlrev_b32_e32 v176, 16, v120
	ds_write_b64 v101, v[172:173] offset:34320
	v_and_b32_e32 v173, 0xffff0000, v118
	v_mul_f32_e32 v176, v168, v176
	v_add_f32_e32 v168, v169, v187
	v_mul_f32_e32 v169, 0x3fb8aa3b, v168
	v_mul_f32_e32 v168, 0xbfb8aa3b, v168
	v_exp_f32_e32 v169, v169
	v_exp_f32_e32 v168, v168
	v_mul_f32_e32 v192, v79, v177
	v_and_b32_e32 v177, 0xffff0000, v120
	v_mul_f32_e32 v173, 0x3d800000, v173
	v_mul_f32_e32 v169, v173, v169
	v_mul_f32_e32 v173, v168, v177
	v_add_f32_e32 v168, v170, v178
	v_mul_f32_e32 v170, 0x3fb8aa3b, v168
	v_mul_f32_e32 v168, 0xbfb8aa3b, v168
	v_exp_f32_e32 v170, v170
	v_exp_f32_e32 v168, v168
	v_lshlrev_b32_e32 v174, 16, v119
	v_mul_f32_e32 v193, v80, v188
	v_lshlrev_b32_e32 v188, 16, v121
	v_mul_f32_e32 v174, 0x3d800000, v174
	v_mul_f32_e32 v170, v174, v170
	v_mul_f32_e32 v174, v168, v188
	v_add_f32_e32 v168, v171, v179
	v_mul_f32_e32 v171, 0x3fb8aa3b, v168
	v_mul_f32_e32 v168, 0xbfb8aa3b, v168
	v_exp_f32_e32 v189, v189
	v_exp_f32_e32 v171, v171
	v_exp_f32_e32 v168, v168
	v_lshlrev_b32_e32 v172, 16, v118
	v_and_b32_e32 v175, 0xffff0000, v119
	v_mul_f32_e32 v194, v78, v191
	v_and_b32_e32 v191, 0xffff0000, v121
	v_mul_f32_e32 v172, 0x3d800000, v172
	v_mul_f32_e32 v175, 0x3d800000, v175
	v_mul_f32_e32 v172, v172, v189
	v_mul_f32_e32 v171, v175, v171
	v_mul_f32_e32 v175, v168, v191
	v_cvt_pk_bf16_f32 v168, v172, v169
	v_cvt_pk_bf16_f32 v169, v170, v171
	v_add_f32_e32 v162, v162, v186
	v_mul_f32_e32 v191, v81, v175
	ds_write_b64 v101, v[168:169] offset:1056
	v_cvt_pk_bf16_f32 v168, v176, v173
	v_cvt_pk_bf16_f32 v169, v174, v175
	v_mul_f32_e32 v175, 0x3fb8aa3b, v162
	v_mul_f32_e32 v162, 0xbfb8aa3b, v162
	v_exp_f32_e32 v162, v162
	s_waitcnt vmcnt(3)
	v_lshlrev_b32_e32 v172, 16, v140
	ds_write_b64 v101, v[168:169] offset:34848
	v_and_b32_e32 v169, 0xffff0000, v130
	v_mul_f32_e32 v172, v162, v172
	v_add_f32_e32 v162, v163, v187
	v_mul_f32_e32 v163, 0x3fb8aa3b, v162
	v_mul_f32_e32 v162, 0xbfb8aa3b, v162
	v_exp_f32_e32 v163, v163
	v_exp_f32_e32 v162, v162
	v_mul_f32_e32 v177, v79, v173
	v_and_b32_e32 v173, 0xffff0000, v140
	v_mul_f32_e32 v169, 0x3d800000, v169
	v_mul_f32_e32 v163, v169, v163
	v_mul_f32_e32 v169, v162, v173
	v_add_f32_e32 v162, v166, v178
	v_mul_f32_e32 v166, 0x3fb8aa3b, v162
	v_mul_f32_e32 v162, 0xbfb8aa3b, v162
	v_exp_f32_e32 v166, v166
	v_exp_f32_e32 v162, v162
	v_lshlrev_b32_e32 v170, 16, v131
	v_mul_f32_e32 v188, v80, v174
	v_lshlrev_b32_e32 v174, 16, v141
	v_mul_f32_e32 v170, 0x3d800000, v170
	v_mul_f32_e32 v166, v170, v166
	v_mul_f32_e32 v170, v162, v174
	v_add_f32_e32 v162, v167, v179
	v_mul_f32_e32 v167, 0x3fb8aa3b, v162
	v_mul_f32_e32 v162, 0xbfb8aa3b, v162
	v_exp_f32_e32 v175, v175
	v_exp_f32_e32 v167, v167
	v_exp_f32_e32 v162, v162
	v_lshlrev_b32_e32 v168, 16, v130
	v_and_b32_e32 v171, 0xffff0000, v131
	v_mul_f32_e32 v189, v78, v176
	v_and_b32_e32 v176, 0xffff0000, v141
	v_mul_f32_e32 v168, 0x3d800000, v168
	v_mul_f32_e32 v171, 0x3d800000, v171
	v_mul_f32_e32 v168, v168, v175
	v_mul_f32_e32 v167, v171, v167
	v_mul_f32_e32 v171, v162, v176
	v_cvt_pk_bf16_f32 v162, v168, v163
	v_cvt_pk_bf16_f32 v163, v166, v167
	v_add_f32_e32 v160, v160, v186
	v_mul_f32_e32 v176, v81, v171
	ds_write_b64 v101, v[162:163] offset:1584
	v_cvt_pk_bf16_f32 v162, v172, v169
	v_cvt_pk_bf16_f32 v163, v170, v171
	v_mul_f32_e32 v171, 0x3fb8aa3b, v160
	v_mul_f32_e32 v160, 0xbfb8aa3b, v160
	v_exp_f32_e32 v160, v160
	v_lshlrev_b32_e32 v168, 16, v134
	v_add_f32_e32 v161, v161, v187
	ds_write_b64 v101, v[162:163] offset:35376
	v_mul_f32_e32 v160, v160, v168
	v_mul_f32_e32 v168, 0x3fb8aa3b, v161
	v_exp_f32_e32 v168, v168
	v_and_b32_e32 v163, 0xffff0000, v132
	v_mul_f32_e32 v163, 0x3d800000, v163
	v_add_f32_e32 v158, v158, v178
	v_mul_f32_e32 v163, v163, v168
	v_mul_f32_e32 v168, 0x3fb8aa3b, v158
	v_mul_f32_e32 v158, 0xbfb8aa3b, v158
	v_exp_f32_e32 v168, v168
	v_exp_f32_e32 v158, v158
	v_lshlrev_b32_e32 v166, 16, v133
	v_mul_f32_e32 v174, v80, v170
	v_lshlrev_b32_e32 v170, 16, v135
	v_mul_f32_e32 v166, 0x3d800000, v166
	v_mul_f32_e32 v166, v166, v168
	v_mul_f32_e32 v168, v158, v170
	v_add_f32_e32 v158, v159, v179
	v_mul_f32_e32 v159, 0x3fb8aa3b, v158
	v_exp_f32_e32 v159, v159
	v_mul_f32_e32 v158, 0xbfb8aa3b, v158
	v_exp_f32_e32 v171, v171
	v_mul_f32_e32 v161, 0xbfb8aa3b, v161
	v_exp_f32_e32 v158, v158
	v_and_b32_e32 v167, 0xffff0000, v133
	v_exp_f32_e32 v161, v161
	v_lshlrev_b32_e32 v162, 16, v132
	v_mul_f32_e32 v167, 0x3d800000, v167
	v_mul_f32_e32 v175, v78, v172
	v_and_b32_e32 v172, 0xffff0000, v135
	v_mul_f32_e32 v162, 0x3d800000, v162
	v_mul_f32_e32 v159, v167, v159
	v_mul_f32_e32 v173, v79, v169
	v_and_b32_e32 v169, 0xffff0000, v134
	v_mul_f32_e32 v162, v162, v171
	v_mul_f32_e32 v167, v158, v172
	v_cvt_pk_bf16_f32 v158, v162, v163
	v_cvt_pk_bf16_f32 v159, v166, v159
	v_add_f32_e32 v156, v156, v186
	v_mul_f32_e32 v161, v161, v169
	v_mul_f32_e32 v172, v81, v167
	ds_write_b64 v101, v[158:159] offset:2112
	v_cvt_pk_bf16_f32 v158, v160, v161
	v_cvt_pk_bf16_f32 v159, v168, v167
	v_mul_f32_e32 v167, 0x3fb8aa3b, v156
	v_mul_f32_e32 v156, 0xbfb8aa3b, v156
	v_exp_f32_e32 v156, v156
	s_waitcnt vmcnt(2)
	v_lshlrev_b32_e32 v162, 16, v142
	v_add_f32_e32 v157, v157, v187
	ds_write_b64 v101, v[158:159] offset:35904
	v_mul_f32_e32 v156, v156, v162
	v_mul_f32_e32 v162, 0x3fb8aa3b, v157
	v_exp_f32_e32 v162, v162
	v_and_b32_e32 v159, 0xffff0000, v136
	v_mul_f32_e32 v159, 0x3d800000, v159
	v_add_f32_e32 v154, v154, v178
	v_mul_f32_e32 v159, v159, v162
	v_mul_f32_e32 v162, 0x3fb8aa3b, v154
	v_mul_f32_e32 v154, 0xbfb8aa3b, v154
	v_exp_f32_e32 v162, v162
	v_exp_f32_e32 v154, v154
	v_mul_f32_e32 v171, v78, v160
	v_lshlrev_b32_e32 v160, 16, v137
	v_lshlrev_b32_e32 v166, 16, v143
	v_mul_f32_e32 v160, 0x3d800000, v160
	v_mul_f32_e32 v160, v160, v162
	v_mul_f32_e32 v162, v154, v166
	v_add_f32_e32 v154, v155, v179
	v_mul_f32_e32 v155, 0x3fb8aa3b, v154
	v_exp_f32_e32 v155, v155
	v_mul_f32_e32 v154, 0xbfb8aa3b, v154
	v_exp_f32_e32 v167, v167
	v_mul_f32_e32 v157, 0xbfb8aa3b, v157
	v_exp_f32_e32 v154, v154
	v_mul_f32_e32 v169, v79, v161
	v_and_b32_e32 v161, 0xffff0000, v137
	v_exp_f32_e32 v157, v157
	v_lshlrev_b32_e32 v158, 16, v136
	v_mul_f32_e32 v161, 0x3d800000, v161
	v_mul_f32_e32 v170, v80, v168
	v_and_b32_e32 v168, 0xffff0000, v143
	v_mul_f32_e32 v158, 0x3d800000, v158
	v_mul_f32_e32 v155, v161, v155
	v_and_b32_e32 v163, 0xffff0000, v142
	v_mul_f32_e32 v158, v158, v167
	v_mul_f32_e32 v161, v154, v168
	v_cvt_pk_bf16_f32 v154, v158, v159
	v_cvt_pk_bf16_f32 v155, v160, v155
	v_add_f32_e32 v152, v152, v186
	v_mul_f32_e32 v157, v157, v163
	v_mul_f32_e32 v168, v81, v161
	ds_write_b64 v101, v[154:155] offset:2640
	v_cvt_pk_bf16_f32 v154, v156, v157
	v_cvt_pk_bf16_f32 v155, v162, v161
	v_mul_f32_e32 v161, 0x3fb8aa3b, v152
	v_mul_f32_e32 v152, 0xbfb8aa3b, v152
	v_exp_f32_e32 v152, v152
	v_lshlrev_b32_e32 v158, 16, v144
	v_add_f32_e32 v153, v153, v187
	ds_write_b64 v101, v[154:155] offset:36432
	v_mul_f32_e32 v152, v152, v158
	v_mul_f32_e32 v158, 0x3fb8aa3b, v153
	v_exp_f32_e32 v158, v158
	v_and_b32_e32 v155, 0xffff0000, v138
	v_mul_f32_e32 v155, 0x3d800000, v155
	v_add_f32_e32 v150, v150, v178
	v_mul_f32_e32 v155, v155, v158
	v_mul_f32_e32 v158, 0x3fb8aa3b, v150
	v_mul_f32_e32 v150, 0xbfb8aa3b, v150
	v_exp_f32_e32 v158, v158
	v_exp_f32_e32 v150, v150
	v_mul_f32_e32 v167, v78, v156
	v_lshlrev_b32_e32 v156, 16, v139
	v_lshlrev_b32_e32 v160, 16, v145
	v_mul_f32_e32 v156, 0x3d800000, v156
	v_mul_f32_e32 v156, v156, v158
	v_mul_f32_e32 v158, v150, v160
	v_add_f32_e32 v150, v151, v179
	v_mul_f32_e32 v151, 0x3fb8aa3b, v150
	v_exp_f32_e32 v151, v151
	v_mul_f32_e32 v150, 0xbfb8aa3b, v150
	v_exp_f32_e32 v161, v161
	v_mul_f32_e32 v153, 0xbfb8aa3b, v153
	v_exp_f32_e32 v150, v150
	v_mul_f32_e32 v163, v79, v157
	v_and_b32_e32 v157, 0xffff0000, v139
	v_exp_f32_e32 v153, v153
	v_lshlrev_b32_e32 v154, 16, v138
	v_mul_f32_e32 v157, 0x3d800000, v157
	v_mul_f32_e32 v166, v80, v162
	v_and_b32_e32 v162, 0xffff0000, v145
	v_mul_f32_e32 v154, 0x3d800000, v154
	v_mul_f32_e32 v151, v157, v151
	v_and_b32_e32 v159, 0xffff0000, v144
	v_mul_f32_e32 v154, v154, v161
	v_mul_f32_e32 v157, v150, v162
	v_cvt_pk_bf16_f32 v150, v154, v155
	v_cvt_pk_bf16_f32 v151, v156, v151
	v_add_f32_e32 v74, v74, v186
	v_mul_f32_e32 v153, v153, v159
	v_mul_f32_e32 v162, v81, v157
	ds_write_b64 v101, v[150:151] offset:3168
	v_cvt_pk_bf16_f32 v150, v152, v153
	v_cvt_pk_bf16_f32 v151, v158, v157
	v_mul_f32_e32 v157, 0x3fb8aa3b, v74
	v_mul_f32_e32 v74, 0xbfb8aa3b, v74
	v_exp_f32_e32 v74, v74
	s_waitcnt vmcnt(0)
	v_lshlrev_b32_e32 v154, 16, v148
	ds_write_b64 v101, v[150:151] offset:36960
	v_and_b32_e32 v151, 0xffff0000, v146
	v_mul_f32_e32 v154, v74, v154
	v_add_f32_e32 v74, v75, v187
	v_mul_f32_e32 v75, 0x3fb8aa3b, v74
	v_mul_f32_e32 v74, 0xbfb8aa3b, v74
	v_exp_f32_e32 v75, v75
	v_exp_f32_e32 v74, v74
	v_and_b32_e32 v155, 0xffff0000, v148
	v_mul_f32_e32 v151, 0x3d800000, v151
	v_mul_f32_e32 v75, v151, v75
	v_mul_f32_e32 v151, v74, v155
	v_add_f32_e32 v74, v76, v178
	v_mul_f32_e32 v76, 0x3fb8aa3b, v74
	v_mul_f32_e32 v74, 0xbfb8aa3b, v74
	v_exp_f32_e32 v76, v76
	v_exp_f32_e32 v74, v74
	v_mul_f32_e32 v161, v78, v152
	v_lshlrev_b32_e32 v152, 16, v147
	v_lshlrev_b32_e32 v156, 16, v149
	v_mul_f32_e32 v152, 0x3d800000, v152
	v_mul_f32_e32 v76, v152, v76
	v_mul_f32_e32 v152, v74, v156
	v_add_f32_e32 v74, v77, v179
	v_mul_f32_e32 v77, 0x3fb8aa3b, v74
	v_mul_f32_e32 v74, 0xbfb8aa3b, v74
	v_exp_f32_e32 v157, v157
	v_exp_f32_e32 v77, v77
	v_exp_f32_e32 v74, v74
	v_mul_f32_e32 v159, v79, v153
	v_lshlrev_b32_e32 v150, 16, v146
	v_and_b32_e32 v153, 0xffff0000, v147
	v_mul_f32_e32 v160, v80, v158
	v_and_b32_e32 v158, 0xffff0000, v149
	v_mul_f32_e32 v150, 0x3d800000, v150
	v_mul_f32_e32 v153, 0x3d800000, v153
	v_mul_f32_e32 v150, v150, v157
	v_mul_f32_e32 v77, v153, v77
	v_mul_f32_e32 v153, v74, v158
	v_cvt_pk_bf16_f32 v74, v150, v75
	v_mul_f32_e32 v155, v79, v151
	v_cvt_pk_bf16_f32 v75, v76, v77
	ds_write_b64 v101, v[74:75] offset:3696
	v_cvt_pk_bf16_f32 v74, v154, v151
	v_lshl_add_u64 v[150:151], v[128:129], 0, s[66:67]
	v_mul_f32_e32 v156, v80, v152
	v_mul_f32_e32 v158, v81, v153
	v_cvt_pk_bf16_f32 v75, v152, v153
	v_or_b32_e32 v152, v150, v84
	v_mov_b32_e32 v153, v151
	v_lshl_add_u64 v[152:153], v[152:153], 4, s[56:57]
	v_mul_f32_e32 v157, v78, v154
	ds_write_b64 v101, v[74:75] offset:37488
	v_cvt_pk_bf16_f32 v74, v197, v194
	v_cvt_pk_bf16_f32 v75, v189, v175
	v_cvt_pk_bf16_f32 v76, v171, v167
	v_cvt_pk_bf16_f32 v77, v161, v157
	global_store_dwordx4 v[152:153], v[74:77], off
	v_or_b32_e32 v152, v150, v100
	v_mov_b32_e32 v153, v151
	v_lshl_add_u64 v[152:153], v[152:153], 4, s[56:57]
	v_cvt_pk_bf16_f32 v74, v190, v192
	v_cvt_pk_bf16_f32 v75, v177, v173
	v_cvt_pk_bf16_f32 v76, v169, v163
	v_cvt_pk_bf16_f32 v77, v159, v155
	global_store_dwordx4 v[152:153], v[74:77], off
	v_or_b32_e32 v152, v150, v102
	v_mov_b32_e32 v153, v151
	v_or_b32_e32 v150, v150, v106
	v_cvt_pk_bf16_f32 v74, v165, v193
	v_cvt_pk_bf16_f32 v75, v188, v174
	v_cvt_pk_bf16_f32 v76, v170, v166
	v_cvt_pk_bf16_f32 v77, v160, v156
	v_lshl_add_u64 v[152:153], v[152:153], 4, s[56:57]
	v_lshl_add_u64 v[150:151], v[150:151], 4, s[56:57]
	global_store_dwordx4 v[152:153], v[74:77], off
	s_nop 1
	v_cvt_pk_bf16_f32 v74, v164, v195
	v_cvt_pk_bf16_f32 v75, v191, v176
	v_cvt_pk_bf16_f32 v76, v172, v168
	v_cvt_pk_bf16_f32 v77, v162, v158
	global_store_dwordx4 v[150:151], v[74:77], off
	s_cbranch_vccnz .LBB0_413
	s_lshl_b64 s[66:67], s[40:41], 10
	v_lshl_add_u64 v[74:75], v[86:87], 0, s[66:67]
	global_store_dwordx4 v[74:75], v[78:81], off
